# v80 + SGPR-base LDS-DMA addressing in the GEMM K-loops + FFN-up epilogue parameter wait moved to first use
# speedup vs baseline: 1.0142x; 1.0019x over previous
.LBB0_360:
	s_mov_b32 s29, -1
	s_ashr_i32 s37, s36, 31
	v_mbcnt_lo_u32_b32 v0, s29, 0
	v_mbcnt_hi_u32_b32 v0, s29, v0
	s_lshl_b64 s[36:37], s[36:37], 7
	v_lshrrev_b32_e32 v46, 1, v0
	s_or_b64 s[36:37], s[36:37], s[80:81]
	v_and_b32_e32 v46, 56, v46
	v_mov_b32_e32 v47, v1
	v_lshl_add_u64 v[182:183], s[36:37], 0, v[46:47]
	v_lshlrev_b64 v[46:47], 2, v[182:183]
	v_lshl_add_u64 v[50:51], s[46:47], 0, v[46:47]
	v_lshl_add_u64 v[58:59], s[52:53], 0, v[46:47]
	v_lshl_add_u64 v[62:63], s[54:55], 0, v[46:47]
	v_lshl_add_u64 v[86:87], s[48:49], 0, v[46:47]
	global_load_dwordx4 v[46:49], v[50:51], off offset:16
	global_load_dwordx4 v[74:77], v[50:51], off
	s_nop 0
	global_load_dwordx4 v[50:53], v[58:59], off offset:16
	global_load_dwordx4 v[78:81], v[58:59], off
	s_nop 0
	global_load_dwordx4 v[58:61], v[62:63], off offset:16
	global_load_dwordx4 v[82:85], v[62:63], off
	s_nop 0
	global_load_dwordx4 v[62:65], v[86:87], off offset:16
	s_nop 0
	global_load_dwordx4 v[86:89], v[86:87], off
	v_ffbh_u32_e32 v192, v191
	v_min_u32_e32 v192, 32, v192
	v_lshlrev_b64 v[190:191], v192, v[190:191]
	v_min_u32_e32 v190, 1, v190
	v_or_b32_e32 v190, v191, v190
	v_ffbh_u32_e32 v191, v189
	v_min_u32_e32 v191, 32, v191
	v_lshlrev_b64 v[188:189], v191, v[188:189]
	v_min_u32_e32 v188, 1, v188
	v_cvt_f32_u32_e32 v190, v190
	v_or_b32_e32 v188, v189, v188
	v_cvt_f32_u32_e32 v188, v188
	v_sub_u32_e32 v189, 32, v192
	v_ldexp_f32 v189, v190, v189
	v_sub_u32_e32 v190, 32, v191
	v_ldexp_f32 v188, v188, v190
	s_mov_b32 s36, 0x32800000
	v_pk_fma_f32 v[192:193], v[188:189], s[36:37], v[196:197] op_sel_hi:[1,0,0]
	s_lshl_b32 s29, s38, 8
	v_mul_f32_e32 v188, 0x4b800000, v193
	v_cmp_gt_f32_e64 s[36:37], s96, v193
	v_readlane_b32 s39, v253, 47
	s_add_i32 s29, s29, s39
	v_cndmask_b32_e64 v188, v193, v188, s[36:37]
	v_rsq_f32_e32 v188, v188
	s_ashr_i32 s39, s38, 31
	v_and_b32_e32 v0, 15, v0
	v_cmp_gt_f32_e32 vcc, s96, v192
	v_mul_f32_e32 v189, 0x45800000, v188
	v_cndmask_b32_e64 v194, v188, v189, s[36:37]
	s_lshl_b64 s[36:37], s[38:39], 2
	s_add_u32 s66, s36, s85
	v_pk_mul_f32 v[188:189], v[194:195], v[160:161] op_sel_hi:[0,1]
	v_pk_mul_f32 v[190:191], v[194:195], v[158:159] op_sel_hi:[0,1]
	v_pk_mul_f32 v[158:159], v[194:195], v[156:157] op_sel_hi:[0,1]
	v_pk_mul_f32 v[160:161], v[194:195], v[154:155] op_sel_hi:[0,1]
	v_or_b32_e32 v193, s29, v0
	s_addc_u32 s67, s37, s84
	v_cmp_lt_u32_e64 s[36:37], 1, v0
	v_mov_b32_dpp v202, v190 row_shr:1 row_mask:0xf bank_mask:0xf bound_ctrl:1
	v_mov_b32_dpp v204, v190 row_shr:2 row_mask:0xf bank_mask:0xf bound_ctrl:1
	v_mov_b32_dpp v203, v191 row_shr:1 row_mask:0xf bank_mask:0xf bound_ctrl:1
	v_mov_b32_dpp v205, v191 row_shr:2 row_mask:0xf bank_mask:0xf bound_ctrl:1
	v_mov_b32_dpp v206, v188 row_shr:1 row_mask:0xf bank_mask:0xf bound_ctrl:1
	v_mov_b32_dpp v208, v188 row_shr:2 row_mask:0xf bank_mask:0xf bound_ctrl:1
	v_mov_b32_dpp v207, v189 row_shr:1 row_mask:0xf bank_mask:0xf bound_ctrl:1
	v_mov_b32_dpp v209, v189 row_shr:2 row_mask:0xf bank_mask:0xf bound_ctrl:1
	v_mov_b32_dpp v210, v160 row_shr:1 row_mask:0xf bank_mask:0xf bound_ctrl:1
	v_mov_b32_dpp v212, v160 row_shr:2 row_mask:0xf bank_mask:0xf bound_ctrl:1
	v_mov_b32_dpp v211, v161 row_shr:1 row_mask:0xf bank_mask:0xf bound_ctrl:1
	v_mov_b32_dpp v213, v161 row_shr:2 row_mask:0xf bank_mask:0xf bound_ctrl:1
	v_mov_b32_dpp v214, v158 row_shr:1 row_mask:0xf bank_mask:0xf bound_ctrl:1
	v_mov_b32_dpp v216, v158 row_shr:2 row_mask:0xf bank_mask:0xf bound_ctrl:1
	v_mov_b32_dpp v215, v159 row_shr:1 row_mask:0xf bank_mask:0xf bound_ctrl:1
	v_mov_b32_dpp v217, v159 row_shr:2 row_mask:0xf bank_mask:0xf bound_ctrl:1
	s_waitcnt vmcnt(0)
	s_and_saveexec_b64 s[38:39], s[36:37]
	s_xor_b64 s[38:39], exec, s[38:39]
	s_cbranch_execz .LBB0_362
	v_pk_fma_f32 v[154:155], v[48:49], v[216:217], v[64:65]
	v_pk_fma_f32 v[212:213], v[46:47], v[212:213], v[62:63]
	v_pk_fma_f32 v[154:155], v[52:53], v[214:215], v[154:155]
	v_pk_fma_f32 v[210:211], v[50:51], v[210:211], v[212:213]
	v_pk_fma_f32 v[154:155], v[158:159], v[60:61], v[154:155]
	v_pk_fma_f32 v[210:211], v[160:161], v[58:59], v[210:211]
	v_mul_f32_e32 v156, 0x3d372713, v154
	v_mul_f32_e32 v157, 0x3d372713, v155
	v_pk_mul_f32 v[200:201], v[194:195], v[148:149] op_sel_hi:[0,1]
	v_mul_f32_e32 v195, 0x3d372713, v210
	v_mul_f32_e32 v156, v154, v156
	v_mul_f32_e32 v157, v155, v157
	v_mul_f32_e32 v195, v210, v195
	v_mul_f32_e32 v212, 0x3d372713, v211
	v_fma_f32 v156, v154, v156, v154
	v_fma_f32 v157, v155, v157, v155
	v_fma_f32 v195, v210, v195, v210
	v_mul_f32_e32 v212, v211, v212
	v_mul_f32_e32 v156, 0xc0135761, v156
	v_mul_f32_e32 v157, 0xc0135761, v157
	v_mul_f32_e32 v195, 0xc0135761, v195
	v_fma_f32 v212, v211, v212, v211
	v_exp_f32_e32 v156, v156
	v_exp_f32_e32 v157, v157
	v_exp_f32_e32 v195, v195
	v_mul_f32_e32 v212, 0xc0135761, v212
	v_exp_f32_e32 v213, v212
	v_add_f32_e32 v156, 1.0, v156
	v_add_f32_e32 v157, 1.0, v157
	v_add_f32_e32 v195, 1.0, v195
	v_rcp_f32_e32 v156, v156
	v_rcp_f32_e32 v157, v157
	v_rcp_f32_e32 v212, v195
	v_add_f32_e32 v195, 1.0, v213
	v_rcp_f32_e32 v213, v195
	v_pk_mul_f32 v[154:155], v[154:155], v[156:157]
	v_pk_fma_f32 v[204:205], v[74:75], v[204:205], v[86:87]
	v_pk_mul_f32 v[200:201], v[200:201], v[154:155]
	v_pk_mul_f32 v[154:155], v[194:195], v[146:147] op_sel_hi:[0,1]
	v_pk_mul_f32 v[156:157], v[210:211], v[212:213]
	v_pk_fma_f32 v[202:203], v[78:79], v[202:203], v[204:205]
	v_pk_mul_f32 v[156:157], v[154:155], v[156:157]
	v_pk_fma_f32 v[154:155], v[76:77], v[208:209], v[88:89]
	v_pk_fma_f32 v[202:203], v[190:191], v[82:83], v[202:203]
	v_pk_fma_f32 v[154:155], v[80:81], v[206:207], v[154:155]
	v_mul_f32_e32 v204, 0x3d372713, v202
	v_pk_fma_f32 v[154:155], v[188:189], v[84:85], v[154:155]
	v_mul_f32_e32 v204, v202, v204
	v_mul_f32_e32 v195, 0x3d372713, v154
	v_mul_f32_e32 v195, v154, v195
	v_mul_f32_e32 v206, 0x3d372713, v155
	v_fma_f32 v195, v154, v195, v154
	v_mul_f32_e32 v206, v155, v206
	v_mul_f32_e32 v195, 0xc0135761, v195
	v_fma_f32 v206, v155, v206, v155
	v_mul_f32_e32 v205, 0x3d372713, v203
	v_exp_f32_e32 v195, v195
	v_mul_f32_e32 v206, 0xc0135761, v206
	v_fma_f32 v204, v202, v204, v202
	v_mul_f32_e32 v205, v203, v205
	v_exp_f32_e32 v207, v206
	v_mul_f32_e32 v204, 0xc0135761, v204
	v_fma_f32 v205, v203, v205, v203
	v_exp_f32_e32 v204, v204
	v_mul_f32_e32 v205, 0xc0135761, v205
	v_exp_f32_e32 v205, v205
	v_add_f32_e32 v195, 1.0, v195
	v_rcp_f32_e32 v206, v195
	v_pk_mul_f32 v[208:209], v[194:195], v[152:153] op_sel_hi:[0,1]
	v_add_f32_e32 v195, 1.0, v207
	v_rcp_f32_e32 v207, v195
	v_add_f32_e32 v195, 1.0, v204
	v_rcp_f32_e32 v204, v195
	v_add_f32_e32 v195, 1.0, v205
	v_rcp_f32_e32 v205, v195
	v_pk_mul_f32 v[154:155], v[154:155], v[206:207]
	v_cvt_pk_bf16_f32 v156, v156, v157
	v_pk_mul_f32 v[206:207], v[208:209], v[154:155]
	v_pk_mul_f32 v[154:155], v[194:195], v[150:151] op_sel_hi:[0,1]
	v_pk_mul_f32 v[194:195], v[202:203], v[204:205]
	v_cvt_pk_bf16_f32 v157, v200, v201
	v_pk_mul_f32 v[154:155], v[154:155], v[194:195]
	v_mov_b64_e32 v[194:195], s[16:17]
	v_cvt_pk_bf16_f32 v154, v154, v155
	v_cvt_pk_bf16_f32 v155, v206, v207
	v_mad_i64_i32 v[200:201], s[40:41], v193, s2, v[194:195]

.LBB0_438:
	v_or_b32_e32 v163, 0x10000, v162
	v_add_u32_e32 v168, 0x10400, v162
	ds_read_b128 v[164:167], v163
	ds_read_b128 v[168:171], v168
	v_add_u32_e32 v163, 0x10800, v162
	v_add_u32_e32 v176, 0x10c00, v162
	s_add_u32 s50, s16, s48
	ds_read_b128 v[172:175], v163
	ds_read_b128 v[176:179], v176
	v_or_b32_e32 v163, 0x14000, v162
	v_add_u32_e32 v184, 0x14400, v162
	s_addc_u32 s51, s17, s49
	ds_read_b128 v[180:183], v163
	ds_read_b128 v[184:187], v184
	v_add_u32_e32 v163, 0x14800, v162
	v_add_u32_e32 v192, 0x14c00, v162
	s_add_u32 s50, s50, 0x100
	ds_read_b128 v[188:191], v163
	ds_read_b128 v[192:195], v192
	s_addc_u32 s51, s51, 0
	s_add_u32 s91, s41, s48
	s_addc_u32 s92, s89, s49
	s_cmpk_eq_i32 s48, 0x700
	s_cselect_b32 s53, s29, s51
	s_cselect_b32 s52, s39, s50
	s_cselect_b32 s51, s45, s92
	s_cselect_b32 s50, s44, s91
	v_lshl_add_u64 v[226:227], v[156:157], 0, s[48:49]
	s_add_i32 m0, s58, 0xc000
	ds_read_b128 v[200:203], v161
	ds_read_b128 v[204:207], v161 offset:1024
	ds_read_b128 v[208:211], v161 offset:2048
	ds_read_b128 v[212:215], v161 offset:3072
	ds_read_b128 v[216:219], v161 offset:4096
	ds_read_b128 v[220:223], v161 offset:5120
	ds_read_b128 v[236:239], v161 offset:6144
	ds_read_b128 v[240:243], v161 offset:7168
	global_load_lds_dwordx4 v[226:227], off
	v_lshl_add_u64 v[226:227], v[158:159], 0, s[48:49]
	s_add_i32 m0, s58, 0xe000
	s_nop 0
	global_load_lds_dwordx4 v[226:227], off
	s_waitcnt vmcnt(8)
	s_waitcnt lgkmcnt(0)
	s_barrier
	s_setprio 1
	s_waitcnt lgkmcnt(0)
	v_mfma_f32_16x16x32_bf16 v[126:129], v[164:167], v[200:203], v[126:129]
	v_mfma_f32_16x16x32_bf16 v[122:125], v[172:175], v[200:203], v[122:125]
	v_mfma_f32_16x16x32_bf16 v[110:113], v[164:167], v[208:211], v[110:113]
	v_mfma_f32_16x16x32_bf16 v[106:109], v[172:175], v[208:211], v[106:109]
	v_mfma_f32_16x16x32_bf16 v[94:97], v[164:167], v[216:219], v[94:97]
	v_mfma_f32_16x16x32_bf16 v[90:93], v[172:175], v[216:219], v[90:93]
	v_mfma_f32_16x16x32_bf16 v[86:89], v[164:167], v[236:239], v[86:89]
	v_mfma_f32_16x16x32_bf16 v[78:81], v[172:175], v[236:239], v[78:81]
	v_mfma_f32_16x16x32_bf16 v[126:129], v[168:171], v[204:207], v[126:129]
	v_mfma_f32_16x16x32_bf16 v[122:125], v[176:179], v[204:207], v[122:125]
	v_mfma_f32_16x16x32_bf16 v[110:113], v[168:171], v[212:215], v[110:113]
	v_mfma_f32_16x16x32_bf16 v[106:109], v[176:179], v[212:215], v[106:109]
	v_mfma_f32_16x16x32_bf16 v[94:97], v[168:171], v[220:223], v[94:97]
	v_mfma_f32_16x16x32_bf16 v[90:93], v[176:179], v[220:223], v[90:93]
	v_mfma_f32_16x16x32_bf16 v[86:89], v[168:171], v[240:243], v[86:89]
	v_mfma_f32_16x16x32_bf16 v[78:81], v[176:179], v[240:243], v[78:81]
	s_setprio 0
	s_setprio 1
	v_mfma_f32_16x16x32_bf16 v[118:121], v[180:183], v[200:203], v[118:121]
	v_mfma_f32_16x16x32_bf16 v[114:117], v[188:191], v[200:203], v[114:117]
	v_mfma_f32_16x16x32_bf16 v[102:105], v[180:183], v[208:211], v[102:105]
	v_mfma_f32_16x16x32_bf16 v[98:101], v[188:191], v[208:211], v[98:101]
	v_mfma_f32_16x16x32_bf16 v[82:85], v[180:183], v[216:219], v[82:85]
	v_mfma_f32_16x16x32_bf16 v[74:77], v[188:191], v[216:219], v[74:77]
	v_mfma_f32_16x16x32_bf16 v[70:73], v[180:183], v[236:239], v[70:73]
	v_mfma_f32_16x16x32_bf16 v[66:69], v[188:191], v[236:239], v[66:69]
	v_mfma_f32_16x16x32_bf16 v[118:121], v[184:187], v[204:207], v[118:121]
	v_mfma_f32_16x16x32_bf16 v[114:117], v[192:195], v[204:207], v[114:117]
	v_mfma_f32_16x16x32_bf16 v[102:105], v[184:187], v[212:215], v[102:105]
	v_mfma_f32_16x16x32_bf16 v[98:101], v[192:195], v[212:215], v[98:101]
	v_mfma_f32_16x16x32_bf16 v[82:85], v[184:187], v[220:223], v[82:85]
	v_mfma_f32_16x16x32_bf16 v[74:77], v[192:195], v[220:223], v[74:77]
	v_mfma_f32_16x16x32_bf16 v[70:73], v[184:187], v[240:243], v[70:73]
	v_mfma_f32_16x16x32_bf16 v[66:69], v[192:195], v[240:243], v[66:69]
	s_setprio 0
	s_barrier
	s_mov_b32 m0, s59
	v_lshl_add_u64 v[226:227], s[50:51], 0, v[0:1]
	s_add_u32 s92, s50, 0x40000
	ds_read_b128 v[200:203], v161 offset:16384
	ds_read_b128 v[204:207], v161 offset:17408
	ds_read_b128 v[208:211], v161 offset:18432
	ds_read_b128 v[212:215], v161 offset:19456
	ds_read_b128 v[216:219], v161 offset:20480
	ds_read_b128 v[220:223], v161 offset:21504
	ds_read_b128 v[236:239], v161 offset:22528
	ds_read_b128 v[240:243], v161 offset:23552
	global_load_lds_dwordx4 v0, s[50:51]
	v_lshl_add_u64 v[244:245], s[50:51], 0, v[142:143]
	s_mov_b32 m0, s60
	s_addc_u32 s93, s51, 0
	global_load_lds_dwordx4 v142, s[50:51]
	s_mov_b32 m0, s61
	v_lshl_add_u64 v[248:249], s[52:53], 0, v[144:145]
	global_load_lds_dwordx4 v0, s[92:93]
	s_mov_b32 m0, s62
	s_nop 0
	global_load_lds_dwordx4 v142, s[92:93]
	v_lshl_add_u64 v[246:247], s[52:53], 0, v[148:149]
	s_mov_b32 m0, s58
	s_nop 0
	global_load_lds_dwordx4 v148, s[52:53]
	s_mov_b32 m0, s63
	s_nop 0
	global_load_lds_dwordx4 v144, s[52:53]
	s_waitcnt vmcnt(8)
	s_waitcnt lgkmcnt(0)
	s_barrier
	s_setprio 1
	s_waitcnt lgkmcnt(0)
	v_mfma_f32_16x16x32_bf16 v[62:65], v[164:167], v[200:203], v[62:65]
	v_mfma_f32_16x16x32_bf16 v[58:61], v[172:175], v[200:203], v[58:61]
	v_mfma_f32_16x16x32_bf16 v[54:57], v[164:167], v[208:211], v[54:57]
	v_mfma_f32_16x16x32_bf16 v[46:49], v[172:175], v[208:211], v[46:49]
	v_mfma_f32_16x16x32_bf16 v[30:33], v[164:167], v[216:219], v[30:33]
	v_mfma_f32_16x16x32_bf16 v[26:29], v[172:175], v[216:219], v[26:29]
	v_mfma_f32_16x16x32_bf16 v[22:25], v[164:167], v[236:239], v[22:25]
	v_mfma_f32_16x16x32_bf16 v[14:17], v[172:175], v[236:239], v[14:17]
	v_mfma_f32_16x16x32_bf16 v[62:65], v[168:171], v[204:207], v[62:65]
	v_mfma_f32_16x16x32_bf16 v[58:61], v[176:179], v[204:207], v[58:61]
	v_mfma_f32_16x16x32_bf16 v[54:57], v[168:171], v[212:215], v[54:57]
	v_mfma_f32_16x16x32_bf16 v[46:49], v[176:179], v[212:215], v[46:49]
	v_mfma_f32_16x16x32_bf16 v[30:33], v[168:171], v[220:223], v[30:33]
	v_mfma_f32_16x16x32_bf16 v[26:29], v[176:179], v[220:223], v[26:29]
	v_mfma_f32_16x16x32_bf16 v[22:25], v[168:171], v[240:243], v[22:25]
	v_mfma_f32_16x16x32_bf16 v[14:17], v[176:179], v[240:243], v[14:17]
	s_setprio 0
	s_setprio 1
	v_mfma_f32_16x16x32_bf16 v[50:53], v[180:183], v[200:203], v[50:53]
	v_mfma_f32_16x16x32_bf16 v[42:45], v[188:191], v[200:203], v[42:45]
	v_mfma_f32_16x16x32_bf16 v[38:41], v[180:183], v[208:211], v[38:41]
	v_mfma_f32_16x16x32_bf16 v[34:37], v[188:191], v[208:211], v[34:37]
	v_mfma_f32_16x16x32_bf16 v[18:21], v[180:183], v[216:219], v[18:21]
	v_mfma_f32_16x16x32_bf16 v[10:13], v[188:191], v[216:219], v[10:13]
	v_mfma_f32_16x16x32_bf16 v[6:9], v[180:183], v[236:239], v[6:9]
	v_mfma_f32_16x16x32_bf16 v[2:5], v[188:191], v[236:239], v[2:5]
	v_mfma_f32_16x16x32_bf16 v[50:53], v[184:187], v[204:207], v[50:53]
	v_mfma_f32_16x16x32_bf16 v[42:45], v[192:195], v[204:207], v[42:45]
	v_mfma_f32_16x16x32_bf16 v[38:41], v[184:187], v[212:215], v[38:41]
	v_mfma_f32_16x16x32_bf16 v[34:37], v[192:195], v[212:215], v[34:37]
	v_mfma_f32_16x16x32_bf16 v[18:21], v[184:187], v[220:223], v[18:21]
	v_mfma_f32_16x16x32_bf16 v[10:13], v[192:195], v[220:223], v[10:13]
	v_mfma_f32_16x16x32_bf16 v[6:9], v[184:187], v[240:243], v[6:9]
	v_mfma_f32_16x16x32_bf16 v[2:5], v[192:195], v[240:243], v[2:5]
	s_setprio 0
	s_barrier
	v_or_b32_e32 v163, 0x18000, v162
	v_add_u32_e32 v168, 0x18400, v162
	ds_read_b128 v[164:167], v163
	ds_read_b128 v[168:171], v168
	v_add_u32_e32 v163, 0x18800, v162
	v_add_u32_e32 v176, 0x18c00, v162
	ds_read_b128 v[172:175], v163
	ds_read_b128 v[176:179], v176
	v_or_b32_e32 v163, 0x1c000, v162
	v_add_u32_e32 v184, 0x1c400, v162
	ds_read_b128 v[180:183], v163
	ds_read_b128 v[184:187], v184
	v_add_u32_e32 v163, 0x1c800, v162
	v_add_u32_e32 v192, 0x1cc00, v162
	ds_read_b128 v[188:191], v163
	ds_read_b128 v[192:195], v192
	s_add_u32 s52, s52, 0x40000
	s_addc_u32 s53, s53, 0
	s_mov_b32 m0, s64
	v_lshl_add_u64 v[228:229], s[52:53], 0, v[148:149]
	ds_read_b128 v[200:203], v161 offset:32768
	ds_read_b128 v[204:207], v161 offset:33792
	ds_read_b128 v[208:211], v161 offset:34816
	ds_read_b128 v[212:215], v161 offset:35840
	ds_read_b128 v[216:219], v161 offset:36864
	ds_read_b128 v[220:223], v161 offset:37888
	ds_read_b128 v[236:239], v161 offset:38912
	ds_read_b128 v[240:243], v161 offset:39936
	global_load_lds_dwordx4 v148, s[52:53]
	v_lshl_add_u64 v[228:229], s[52:53], 0, v[144:145]
	s_mov_b32 m0, s65
	s_nop 0
	global_load_lds_dwordx4 v144, s[52:53]
	s_waitcnt vmcnt(8)
	s_waitcnt lgkmcnt(0)
	s_barrier
	s_setprio 1
	s_waitcnt lgkmcnt(0)
	v_mfma_f32_16x16x32_bf16 v[126:129], v[164:167], v[200:203], v[126:129]
	v_mfma_f32_16x16x32_bf16 v[122:125], v[172:175], v[200:203], v[122:125]
	v_mfma_f32_16x16x32_bf16 v[110:113], v[164:167], v[208:211], v[110:113]
	v_mfma_f32_16x16x32_bf16 v[106:109], v[172:175], v[208:211], v[106:109]
	v_mfma_f32_16x16x32_bf16 v[94:97], v[164:167], v[216:219], v[94:97]
	v_mfma_f32_16x16x32_bf16 v[90:93], v[172:175], v[216:219], v[90:93]
	v_mfma_f32_16x16x32_bf16 v[86:89], v[164:167], v[236:239], v[86:89]
	v_mfma_f32_16x16x32_bf16 v[78:81], v[172:175], v[236:239], v[78:81]
	v_mfma_f32_16x16x32_bf16 v[126:129], v[168:171], v[204:207], v[126:129]
	v_mfma_f32_16x16x32_bf16 v[122:125], v[176:179], v[204:207], v[122:125]
	v_mfma_f32_16x16x32_bf16 v[110:113], v[168:171], v[212:215], v[110:113]
	v_mfma_f32_16x16x32_bf16 v[106:109], v[176:179], v[212:215], v[106:109]
	v_mfma_f32_16x16x32_bf16 v[94:97], v[168:171], v[220:223], v[94:97]
	v_mfma_f32_16x16x32_bf16 v[90:93], v[176:179], v[220:223], v[90:93]
	v_mfma_f32_16x16x32_bf16 v[86:89], v[168:171], v[240:243], v[86:89]
	v_mfma_f32_16x16x32_bf16 v[78:81], v[176:179], v[240:243], v[78:81]
	s_setprio 0
	s_setprio 1
	v_mfma_f32_16x16x32_bf16 v[118:121], v[180:183], v[200:203], v[118:121]
	v_mfma_f32_16x16x32_bf16 v[114:117], v[188:191], v[200:203], v[114:117]
	v_mfma_f32_16x16x32_bf16 v[102:105], v[180:183], v[208:211], v[102:105]
	v_mfma_f32_16x16x32_bf16 v[98:101], v[188:191], v[208:211], v[98:101]
	v_mfma_f32_16x16x32_bf16 v[82:85], v[180:183], v[216:219], v[82:85]
	v_mfma_f32_16x16x32_bf16 v[74:77], v[188:191], v[216:219], v[74:77]
	v_mfma_f32_16x16x32_bf16 v[70:73], v[180:183], v[236:239], v[70:73]
	v_mfma_f32_16x16x32_bf16 v[66:69], v[188:191], v[236:239], v[66:69]
	v_mfma_f32_16x16x32_bf16 v[118:121], v[184:187], v[204:207], v[118:121]
	v_mfma_f32_16x16x32_bf16 v[114:117], v[192:195], v[204:207], v[114:117]
	v_mfma_f32_16x16x32_bf16 v[102:105], v[184:187], v[212:215], v[102:105]
	v_mfma_f32_16x16x32_bf16 v[98:101], v[192:195], v[212:215], v[98:101]
	v_mfma_f32_16x16x32_bf16 v[82:85], v[184:187], v[220:223], v[82:85]
	v_mfma_f32_16x16x32_bf16 v[74:77], v[192:195], v[220:223], v[74:77]
	v_mfma_f32_16x16x32_bf16 v[70:73], v[184:187], v[240:243], v[70:73]
	v_mfma_f32_16x16x32_bf16 v[66:69], v[192:195], v[240:243], v[66:69]
	s_setprio 0
	s_barrier
	s_mov_b32 m0, s66
	v_lshl_add_u64 v[226:227], v[226:227], 0, s[18:19]
	s_add_u32 s50, s50, 0x40080
	ds_read_b128 v[200:203], v161 offset:49152
	ds_read_b128 v[204:207], v161 offset:50176
	ds_read_b128 v[208:211], v161 offset:51200
	ds_read_b128 v[212:215], v161 offset:52224
	ds_read_b128 v[216:219], v161 offset:53248
	ds_read_b128 v[220:223], v161 offset:54272
	ds_read_b128 v[236:239], v161 offset:55296
	ds_read_b128 v[240:243], v161 offset:56320
	global_load_lds_dwordx4 v[226:227], off
	v_lshl_add_u64 v[226:227], v[244:245], 0, s[18:19]
	s_mov_b32 m0, s67
	s_addc_u32 s51, s51, 0
	global_load_lds_dwordx4 v[226:227], off
	s_mov_b32 m0, s83
	s_nop 0
	global_load_lds_dwordx4 v0, s[50:51]
	s_mov_b32 m0, s84
	s_nop 0
	global_load_lds_dwordx4 v142, s[50:51]
	v_lshl_add_u64 v[226:227], v[246:247], 0, s[18:19]
	s_mov_b32 m0, s80
	s_nop 0
	global_load_lds_dwordx4 v[226:227], off
	v_lshl_add_u64 v[226:227], v[248:249], 0, s[18:19]
	s_mov_b32 m0, s82
	s_nop 0
	global_load_lds_dwordx4 v[226:227], off
	s_waitcnt vmcnt(8)
	s_waitcnt lgkmcnt(0)
	s_barrier
	s_setprio 1
	s_waitcnt lgkmcnt(0)
	v_mfma_f32_16x16x32_bf16 v[62:65], v[164:167], v[200:203], v[62:65]
	v_mfma_f32_16x16x32_bf16 v[58:61], v[172:175], v[200:203], v[58:61]
	v_mfma_f32_16x16x32_bf16 v[54:57], v[164:167], v[208:211], v[54:57]
	v_mfma_f32_16x16x32_bf16 v[46:49], v[172:175], v[208:211], v[46:49]
	v_mfma_f32_16x16x32_bf16 v[30:33], v[164:167], v[216:219], v[30:33]
	v_mfma_f32_16x16x32_bf16 v[26:29], v[172:175], v[216:219], v[26:29]
	v_mfma_f32_16x16x32_bf16 v[22:25], v[164:167], v[236:239], v[22:25]
	v_mfma_f32_16x16x32_bf16 v[14:17], v[172:175], v[236:239], v[14:17]
	v_mfma_f32_16x16x32_bf16 v[62:65], v[168:171], v[204:207], v[62:65]
	v_mfma_f32_16x16x32_bf16 v[58:61], v[176:179], v[204:207], v[58:61]
	v_mfma_f32_16x16x32_bf16 v[54:57], v[168:171], v[212:215], v[54:57]
	v_mfma_f32_16x16x32_bf16 v[46:49], v[176:179], v[212:215], v[46:49]
	v_mfma_f32_16x16x32_bf16 v[30:33], v[168:171], v[220:223], v[30:33]
	v_mfma_f32_16x16x32_bf16 v[26:29], v[176:179], v[220:223], v[26:29]
	v_mfma_f32_16x16x32_bf16 v[22:25], v[168:171], v[240:243], v[22:25]
	v_mfma_f32_16x16x32_bf16 v[14:17], v[176:179], v[240:243], v[14:17]
	s_setprio 0
	s_setprio 1
	v_mfma_f32_16x16x32_bf16 v[50:53], v[180:183], v[200:203], v[50:53]
	v_mfma_f32_16x16x32_bf16 v[42:45], v[188:191], v[200:203], v[42:45]
	v_mfma_f32_16x16x32_bf16 v[38:41], v[180:183], v[208:211], v[38:41]
	v_mfma_f32_16x16x32_bf16 v[34:37], v[188:191], v[208:211], v[34:37]
	v_mfma_f32_16x16x32_bf16 v[18:21], v[180:183], v[216:219], v[18:21]
	v_mfma_f32_16x16x32_bf16 v[10:13], v[188:191], v[216:219], v[10:13]
	v_mfma_f32_16x16x32_bf16 v[6:9], v[180:183], v[236:239], v[6:9]
	v_mfma_f32_16x16x32_bf16 v[2:5], v[188:191], v[236:239], v[2:5]
	v_mfma_f32_16x16x32_bf16 v[50:53], v[184:187], v[204:207], v[50:53]
	v_mfma_f32_16x16x32_bf16 v[42:45], v[192:195], v[204:207], v[42:45]
	v_mfma_f32_16x16x32_bf16 v[38:41], v[184:187], v[212:215], v[38:41]
	v_mfma_f32_16x16x32_bf16 v[34:37], v[192:195], v[212:215], v[34:37]
	v_mfma_f32_16x16x32_bf16 v[18:21], v[184:187], v[220:223], v[18:21]
	v_mfma_f32_16x16x32_bf16 v[10:13], v[192:195], v[220:223], v[10:13]
	v_mfma_f32_16x16x32_bf16 v[6:9], v[184:187], v[240:243], v[6:9]
	v_mfma_f32_16x16x32_bf16 v[2:5], v[192:195], v[240:243], v[2:5]
	s_setprio 0
	s_barrier
	s_add_i32 s90, s90, 2
	s_add_u32 s48, s48, 0x100
	s_addc_u32 s49, s49, 0
	s_cmp_gt_u32 s90, 13
	s_cbranch_scc0 .LBB0_438
	s_add_u32 s48, s41, 0xffffff00
	s_addc_u32 s49, s89, -1
	s_and_b64 vcc, exec, s[36:37]
	s_movk_i32 s90, 0xfea0
	s_cbranch_vccnz .LBB0_441
	v_lshl_add_u32 v2, s38, 8, v160
	v_ashrrev_i32_e32 v3, 31, v2
	v_lshl_add_u64 v[2:3], v[2:3], 3, s[14:15]
	global_load_dwordx2 v[150:151], v[2:3], off nt
	global_load_dwordx2 v[146:147], v[2:3], off offset:128 nt
	global_load_dwordx2 v[140:141], v[2:3], off offset:256 nt
	global_load_dwordx2 v[138:139], v[2:3], off offset:384 nt
	global_load_dwordx2 v[136:137], v[2:3], off offset:1024 nt
	global_load_dwordx2 v[134:135], v[2:3], off offset:1152 nt
	global_load_dwordx2 v[132:133], v[2:3], off offset:1280 nt
	global_load_dwordx2 v[130:131], v[2:3], off offset:1408 nt
	v_mov_b32_e32 v2, 0
	s_mov_b32 s0, s40
	s_mov_b32 s34, s38
	s_mov_b64 s[16:17], s[46:47]
	s_mov_b32 s85, s88
	v_mov_b32_e32 v3, v2
	v_mov_b64_e32 v[4:5], v[2:3]
	v_mov_b64_e32 v[6:7], v[2:3]
	v_mov_b64_e32 v[8:9], v[2:3]
	v_mov_b64_e32 v[10:11], v[2:3]
	v_mov_b64_e32 v[12:13], v[2:3]
	v_mov_b64_e32 v[14:15], v[2:3]
	v_mov_b64_e32 v[16:17], v[2:3]
	v_mov_b64_e32 v[18:19], v[2:3]
	v_mov_b64_e32 v[20:21], v[2:3]
	v_mov_b64_e32 v[22:23], v[2:3]
	v_mov_b64_e32 v[24:25], v[2:3]
	v_mov_b64_e32 v[26:27], v[2:3]
	v_mov_b64_e32 v[28:29], v[2:3]
	v_mov_b64_e32 v[30:31], v[2:3]
	v_mov_b64_e32 v[32:33], v[2:3]
	v_mov_b64_e32 v[34:35], v[2:3]
	v_mov_b64_e32 v[36:37], v[2:3]
	v_mov_b64_e32 v[38:39], v[2:3]
	v_mov_b64_e32 v[40:41], v[2:3]
	v_mov_b64_e32 v[42:43], v[2:3]
	v_mov_b64_e32 v[44:45], v[2:3]
	v_mov_b64_e32 v[46:47], v[2:3]
	v_mov_b64_e32 v[48:49], v[2:3]
	v_mov_b64_e32 v[50:51], v[2:3]
	v_mov_b64_e32 v[52:53], v[2:3]
	v_mov_b64_e32 v[54:55], v[2:3]
	v_mov_b64_e32 v[56:57], v[2:3]
	v_mov_b64_e32 v[58:59], v[2:3]
	v_mov_b64_e32 v[60:61], v[2:3]
	v_mov_b64_e32 v[62:63], v[2:3]
	v_mov_b64_e32 v[64:65], v[2:3]
	v_mov_b64_e32 v[66:67], v[2:3]
	v_mov_b64_e32 v[68:69], v[2:3]
	v_mov_b64_e32 v[70:71], v[2:3]
	v_mov_b64_e32 v[72:73], v[2:3]
	v_mov_b64_e32 v[74:75], v[2:3]
	v_mov_b64_e32 v[76:77], v[2:3]
	v_mov_b64_e32 v[78:79], v[2:3]
	v_mov_b64_e32 v[80:81], v[2:3]
	v_mov_b64_e32 v[82:83], v[2:3]
	v_mov_b64_e32 v[84:85], v[2:3]
	v_mov_b64_e32 v[86:87], v[2:3]
	v_mov_b64_e32 v[88:89], v[2:3]
	v_mov_b64_e32 v[90:91], v[2:3]
	v_mov_b64_e32 v[92:93], v[2:3]
	v_mov_b64_e32 v[94:95], v[2:3]
	v_mov_b64_e32 v[96:97], v[2:3]
	v_mov_b64_e32 v[98:99], v[2:3]
	v_mov_b64_e32 v[100:101], v[2:3]
	v_mov_b64_e32 v[102:103], v[2:3]
	v_mov_b64_e32 v[104:105], v[2:3]
	v_mov_b64_e32 v[106:107], v[2:3]
	v_mov_b64_e32 v[108:109], v[2:3]
	v_mov_b64_e32 v[110:111], v[2:3]
	v_mov_b64_e32 v[112:113], v[2:3]
	v_mov_b64_e32 v[114:115], v[2:3]
	v_mov_b64_e32 v[116:117], v[2:3]
	v_mov_b64_e32 v[118:119], v[2:3]
	v_mov_b64_e32 v[120:121], v[2:3]
	v_mov_b64_e32 v[122:123], v[2:3]
	v_mov_b64_e32 v[124:125], v[2:3]
	v_mov_b64_e32 v[126:127], v[2:3]
	v_mov_b64_e32 v[128:129], v[2:3]
	s_branch .LBB0_442
